# prologue: context hyena filter tasks 512-519 run on workgroups 192-199 (no modulation-vector task there) instead of 0-7
# baseline (speedup 1.0000x reference)
;     ...
;     ((float*)(P.ws + WS_NORMP))[(size_t)tid * 520 + task] = asum;
;     ...
;         for (int task = bid; task < 520; task += nb) hyena_filter_task(P, sm, task, rep == 0 ? 1 : 0);
.LBB0_36:
	s_ashr_i32 s15, s14, 31
	v_readlane_b32 s0, v253, 10
	v_lshl_add_u64 v[2:3], s[14:15], 2, v[14:15]
	v_readlane_b32 s1, v253, 11
	global_store_dword v[2:3], v22, off
	s_add_i32 s14, s14, s0
	s_cmpk_lg_u32 s0, 0x100
	s_cbranch_scc1 .Lhyd_orig
	s_cmpk_lt_i32 s14, 0x200
	s_cbranch_scc1 .LBB0_37
	s_addk_i32 s14, 0xff40
	s_cmpk_lt_i32 s14, 0x200
	s_cbranch_scc1 .LBB0_109
.Lhyd_orig:
	s_cmpk_gt_i32 s14, 0x207
	s_cbranch_scc1 .LBB0_109
